# LN2 row loop (layers 0-2): next layer's shift/scale vectors staged per wave in LDS with LDS-DMA loads when the sample changes, read back with ds_read_b128 every row (8 fewer global loads per row)
# speedup vs baseline: 1.0117x; 1.0013x over previous
; #define GAS __attribute__((address_space(1)))
; __device__ __forceinline__ void ph_ln2(Frame& F, int l, int ntok, bool last) {
;     const int gw = F.wg * NWAVES + F.wave, NGW = F.G * NWAVES;
;     const int cA = 256 * (F.lane >> 4) + 32 * ((F.lane >> 2) & 3) + 8 * (F.lane & 3);
;     ...
;     const float* lg = F.in[I_LN2G] + l * DM; const float* lb = F.in[I_LN2B] + l * DM;
;     struct Ln2Raw { u32x2 q[8]; u32x4 qs, xa, xb; };
;     auto ln2_load = [&](int row) { Ln2Raw r;
;         const unsigned char* y2 = (const unsigned char*)(F.ws + WS_Y2) + (size_t)row * 5120;
;         const bf16_t* xr = (const bf16_t*)(F.ws + WS_XR) + (size_t)row * DM;
; #pragma unroll
;         for (int k = 0; k < 8; ++k) r.q[k] = __builtin_nontemporal_load((const GAS u32x2*)(y2 + k * 512 + 8 * F.lane));
;         r.qs = __builtin_nontemporal_load((const GAS u32x4*)(y2 + 4096 + 16 * F.lane));
;         r.xa = __builtin_nontemporal_load((const GAS u32x4*)(xr + cA)); r.xb = __builtin_nontemporal_load((const GAS u32x4*)(xr + cA + 128));
;         return r; };
;     Ln2Raw cur = ln2_load(gw < ntok ? gw : 0);
.LBB0_1687:
	v_readlane_b32 s36, v252, 8
	s_mov_b32 s0, s97
	v_readlane_b32 s38, v252, 10
	v_readlane_b32 s39, v252, 11
	v_readlane_b32 s4, v254, 28
	v_mbcnt_lo_u32_b32 v8, -1, 0
	v_mbcnt_hi_u32_b32 v8, -1, v8
	v_readlane_b32 s37, v252, 9
	s_mov_b64 s[20:21], s[38:39]
	s_add_i32 s38, s0, s4
	s_mov_b64 s[2:3], s[36:37]
	s_cmp_ge_i32 s38, s80
	s_cbranch_scc1 .LBB0_1696
	s_lshl_b32 s22, s30, 10
	v_readlane_b32 s40, v252, 0
	s_lshl_b64 s[4:5], s[22:23], 2
	v_readlane_b32 s46, v252, 6
	v_readlane_b32 s47, v252, 7
	s_add_u32 s18, s46, s4
	v_readlane_b32 s44, v252, 4
	s_addc_u32 s19, s47, s5
	v_readlane_b32 s45, v252, 5
	s_add_u32 s4, s44, s4
	s_addc_u32 s5, s45, s5
	s_add_u32 s36, s20, 0x64000000
	v_lshlrev_b32_e32 v34, 3, v8
	v_readlane_b32 s42, v252, 2
	v_readlane_b32 s43, v252, 3
	s_addc_u32 s37, s21, 0
	s_ashr_i32 s39, s38, 31
	v_lshlrev_b32_e32 v32, 4, v8
	v_and_b32_e32 v0, 0x78, v34
	s_movk_i32 s0, 0xff00
	s_lshl_b64 s[42:43], s[38:39], 11
	v_and_or_b32 v36, v32, s0, v0
	v_readlane_b32 s41, v252, 1
	s_add_u32 s40, s36, s42
	v_ashrrev_i32_e32 v37, 31, v36
	s_addc_u32 s41, s37, s43
	v_lshlrev_b64 v[10:11], 1, v[36:37]
	s_add_u32 s22, s20, 0x2f600000
	v_lshl_add_u64 v[0:1], s[40:41], 0, v[10:11]
	s_addc_u32 s44, s21, 0
	s_mul_i32 s40, s38, 0x1400
	s_mul_hi_i32 s0, s38, 0x1400
	s_add_u32 s40, s22, s40
	s_addc_u32 s41, s44, s0
	v_ashrrev_i32_e32 v33, 31, v32
	s_waitcnt vmcnt(0)
	v_lshl_add_u64 v[4:5], s[40:41], 0, v[32:33]
	s_movk_i32 s0, 0x1000
	v_add_co_u32_e32 v4, vcc, s0, v4
	v_ashrrev_i32_e32 v35, 31, v34
	s_nop 0
	v_addc_co_u32_e32 v5, vcc, 0, v5, vcc
	v_lshl_add_u64 v[16:17], s[40:41], 0, v[34:35]
	global_load_dwordx4 v[12:15], v[0:1], off offset:256 nt
	s_nop 0
	global_load_dwordx4 v[0:3], v[0:1], off nt
	s_nop 0
	global_load_dwordx2 v[66:67], v[16:17], off offset:3584 nt
	global_load_dwordx2 v[64:65], v[16:17], off offset:3072 nt
	global_load_dwordx2 v[62:63], v[16:17], off offset:2560 nt
	global_load_dwordx2 v[60:61], v[16:17], off offset:2048 nt
	global_load_dwordx2 v[58:59], v[16:17], off offset:1536 nt
	global_load_dwordx2 v[56:57], v[16:17], off offset:1024 nt
	global_load_dwordx2 v[54:55], v[16:17], off offset:512 nt
	s_nop 0
	global_load_dwordx4 v[4:7], v[4:5], off nt
	s_nop 0
	global_load_dwordx2 v[52:53], v[16:17], off nt
	s_mul_i32 s45, s30, 17
	s_add_i32 s46, s45, 17
	v_lshlrev_b64 v[40:41], 2, v[36:37]
	s_add_u32 s47, s20, 0x100000
	v_lshl_add_u64 v[42:43], s[4:5], 0, v[40:41]
	s_addc_u32 s48, s21, 0
	s_lshl_b64 s[40:41], s[38:39], 5
	s_lshl_b64 s[4:5], s[38:39], 12
	s_add_u32 s2, s2, s4
	v_or_b32_e32 v38, 0x80, v36
	v_lshlrev_b32_e32 v8, 2, v8
	s_addc_u32 s3, s3, s5
	v_ashrrev_i32_e32 v39, 31, v38
	v_lshl_add_u64 v[44:45], s[18:19], 0, v[40:41]
	v_lshl_add_u64 v[46:47], s[36:37], 0, v[10:11]
	v_xor_b32_e32 v103, 4, v8
	v_xor_b32_e32 v107, 8, v8
	v_xor_b32_e32 v113, 16, v8
	v_xor_b32_e32 v170, 32, v8
	v_xor_b32_e32 v171, 64, v8
	v_xor_b32_e32 v172, 0x80, v8
	v_lshl_add_u64 v[48:49], s[2:3], 0, v[40:41]
	v_lshl_add_u64 v[50:51], s[42:43], 0, v[10:11]
	global_load_dwordx4 v[182:185], v[42:43], off offset:16
	global_load_dwordx4 v[186:189], v[42:43], off
	global_load_dwordx4 v[194:197], v[44:45], off offset:16
	global_load_dwordx4 v[198:201], v[44:45], off
	global_load_dwordx4 v[202:205], v[42:43], off offset:528
	global_load_dwordx4 v[216:219], v[42:43], off offset:512
	global_load_dwordx4 v[220:223], v[44:45], off offset:528
	global_load_dwordx4 v[236:239], v[44:45], off offset:512
	s_mov_b32 s88, 1
	s_mov_b32 s89, 1
	s_branch .LBB0_1690

; #define GAS __attribute__((address_space(1)))
; __device__ __forceinline__ unsigned pk2(float lo, float hi) { const f32x2 v = {lo, hi}; const bf16v2 b = __builtin_convertvector(v, bf16v2); return __builtin_bit_cast(unsigned, b); }
; __device__ __forceinline__ const float* mod_ptr(const Frame& F, int l, int row) { return (const float*)(F.ws + WS_MOD) + ((size_t)l * 17 + row_b(row)) * 6144; }
; __device__ __forceinline__ void ph_ln2(Frame& F, int l, int ntok, bool last) {
;     ...
;         const float rstd = 1.f / sqrtf(wave_sum(s2, F.lane) * (1.f / DM) + LN_EPS);
;         const float* mdn = last ? md : mod_ptr(F, l + 1, row);
;         float xn[16];
; #pragma unroll
;         for (int j = 0; j < 4; ++j) { const f32x4 g = *(const GAS f32x4*)(lg + LN2_COL(j)), bb = *(const GAS f32x4*)(lb + LN2_COL(j));
; #pragma unroll
;             for (int e = 0; e < 4; ++e) xn[4 * j + e] = v[4 * j + e] * rstd * g[e] + bb[e]; }
;         if (last) { float* op = F.out + (size_t)row * DM;
; #pragma unroll
;             for (int j = 0; j < 4; ++j) *(GAS f32x4*)(op + LN2_COL(j)) = (f32x4){xn[4 * j], xn[4 * j + 1], xn[4 * j + 2], xn[4 * j + 3]}; }
;         else {
;             __builtin_nontemporal_store((u32x4){pk2(xn[0], xn[1]), pk2(xn[2], xn[3]), pk2(xn[4], xn[5]), pk2(xn[6], xn[7])}, (GAS u32x4*)(xr + cA)); __builtin_nontemporal_store((u32x4){pk2(xn[8], xn[9]), pk2(xn[10], xn[11]), pk2(xn[12], xn[13]), pk2(xn[14], xn[15])}, (GAS u32x4*)(xr + cA + 128));
;             bf16_t* xm = (bf16_t*)(F.ws + WS_XM) + (size_t)row * DM;
;             unsigned w[8];
; #pragma unroll
;             for (int j = 0; j < 4; ++j) { const f32x4 sh = *(const GAS f32x4*)(mdn + LN2_COL(j)), sc = *(const GAS f32x4*)(mdn + 1024 + LN2_COL(j));
;                 w[2 * j] = pk2(xn[4 * j] * (1.f + sc[0]) + sh[0], xn[4 * j + 1] * (1.f + sc[1]) + sh[1]); w[2 * j + 1] = pk2(xn[4 * j + 2] * (1.f + sc[2]) + sh[2], xn[4 * j + 3] * (1.f + sc[3]) + sh[3]); }
;             *(GAS u32x4*)(xm + cA) = (u32x4){w[0], w[1], w[2], w[3]}; *(GAS u32x4*)(xm + cA + 128) = (u32x4){w[4], w[5], w[6], w[7]};
.LBB0_1692:
	s_waitcnt lgkmcnt(0)
	v_add_f32_e32 v16, v16, v17
	v_fmamk_f32 v16, v16, 0x3a800000, v234
	s_mov_b32 s0, 0xf800000
	v_cmp_gt_f32_e32 vcc, s0, v16
	v_mul_f32_e32 v17, 0x4f800000, v16
	s_nop 0
	v_cndmask_b32_e32 v16, v16, v17, vcc
	v_sqrt_f32_e32 v17, v16
	s_nop 0
	v_add_u32_e32 v18, -1, v17
	v_fma_f32 v19, -v18, v17, v16
	v_cmp_ge_f32_e64 s[36:37], 0, v19
	v_add_u32_e32 v19, 1, v17
	s_nop 0
	v_cndmask_b32_e64 v18, v17, v18, s[36:37]
	v_fma_f32 v17, -v19, v17, v16
	v_cmp_lt_f32_e64 s[36:37], 0, v17
	s_nop 1
	v_cndmask_b32_e64 v17, v18, v19, s[36:37]
	v_mul_f32_e32 v18, 0x37800000, v17
	v_cndmask_b32_e32 v17, v17, v18, vcc
	v_cmp_class_f32_e32 vcc, v16, v232
	s_mov_b64 s[36:37], -1
	s_nop 0
	v_cndmask_b32_e32 v16, v17, v16, vcc
	v_div_scale_f32 v17, s[4:5], v16, v16, 1.0
	v_rcp_f32_e32 v18, v17
	v_readlane_b32 s4, v255, 32
	v_readlane_b32 s5, v255, 33
	v_fma_f32 v19, -v17, v18, 1.0
	v_fmac_f32_e32 v18, v19, v18
	v_div_scale_f32 v19, vcc, 1.0, v16, 1.0
	v_mul_f32_e32 v68, v19, v18
	v_fma_f32 v69, -v17, v68, v19
	v_fmac_f32_e32 v68, v69, v18
	v_fma_f32 v17, -v17, v68, v19
	v_div_fmas_f32 v17, v17, v18, v68
	v_div_fixup_f32 v80, v17, v16, 1.0
	v_mov_b32_e32 v68, v182
	v_mov_b32_e32 v69, v183
	v_mov_b32_e32 v70, v184
	v_mov_b32_e32 v71, v185
	v_mov_b32_e32 v16, v186
	v_mov_b32_e32 v17, v187
	v_mov_b32_e32 v18, v188
	v_mov_b32_e32 v19, v189
	v_mov_b32_e32 v72, v194
	v_mov_b32_e32 v73, v195
	v_mov_b32_e32 v74, v196
	v_mov_b32_e32 v75, v197
	v_mov_b32_e32 v76, v198
	v_mov_b32_e32 v77, v199
	v_mov_b32_e32 v78, v200
	v_mov_b32_e32 v79, v201
	v_pk_mul_f32 v[12:13], v[12:13], v[80:81] op_sel_hi:[1,0]
	v_pk_mul_f32 v[20:21], v[20:21], v[80:81] op_sel_hi:[1,0]
	s_and_b64 vcc, exec, s[4:5]
	s_waitcnt vmcnt(0)
	v_pk_fma_f32 v[16:17], v[12:13], v[16:17], v[76:77]
	v_pk_mul_f32 v[12:13], v[14:15], v[80:81] op_sel_hi:[1,0]
	v_pk_mul_f32 v[14:15], v[26:27], v[80:81] op_sel_hi:[1,0]
	v_pk_fma_f32 v[18:19], v[12:13], v[18:19], v[78:79]
	v_pk_mul_f32 v[12:13], v[24:25], v[80:81] op_sel_hi:[1,0]
	v_pk_fma_f32 v[14:15], v[14:15], v[70:71], v[74:75]
	v_pk_fma_f32 v[12:13], v[12:13], v[68:69], v[72:73]
	v_mov_b32_e32 v68, v202
	v_mov_b32_e32 v69, v203
	v_mov_b32_e32 v70, v204
	v_mov_b32_e32 v71, v205
	v_mov_b32_e32 v24, v216
	v_mov_b32_e32 v25, v217
	v_mov_b32_e32 v26, v218
	v_mov_b32_e32 v27, v219
	v_mov_b32_e32 v72, v220
	v_mov_b32_e32 v73, v221
	v_mov_b32_e32 v74, v222
	v_mov_b32_e32 v75, v223
	v_mov_b32_e32 v76, v236
	v_mov_b32_e32 v77, v237
	v_mov_b32_e32 v78, v238
	v_mov_b32_e32 v79, v239
	s_waitcnt vmcnt(0)
	v_pk_fma_f32 v[24:25], v[20:21], v[24:25], v[76:77]
	v_pk_mul_f32 v[20:21], v[22:23], v[80:81] op_sel_hi:[1,0]
	v_pk_mul_f32 v[22:23], v[30:31], v[80:81] op_sel_hi:[1,0]
	v_pk_fma_f32 v[26:27], v[20:21], v[26:27], v[78:79]
	v_pk_mul_f32 v[20:21], v[28:29], v[80:81] op_sel_hi:[1,0]
	v_pk_fma_f32 v[22:23], v[22:23], v[70:71], v[74:75]
	v_pk_fma_f32 v[20:21], v[20:21], v[68:69], v[72:73]
	s_cbranch_vccz .LBB0_1694
	v_lshl_add_u64 v[84:85], s[20:21], 0, v[50:51]
	v_add_co_u32_e32 v68, vcc, 0x64000000, v84
	v_cvt_pk_bf16_f32 v28, v16, v17
	v_cvt_pk_bf16_f32 v29, v18, v19
	v_cvt_pk_bf16_f32 v30, v12, v13
	v_cvt_pk_bf16_f32 v31, v14, v15
	v_addc_co_u32_e32 v69, vcc, 0, v85, vcc
	s_add_u32 s36, s2, 0x1000
	global_store_dwordx4 v[68:69], v[28:31], off nt
	s_addc_u32 s37, s3, 0
	v_lshl_add_u64 v[80:81], s[2:3], 0, v[40:41]
	v_cvt_pk_bf16_f32 v28, v24, v25
	v_cvt_pk_bf16_f32 v29, v26, v27
	v_cvt_pk_bf16_f32 v30, v20, v21
	v_cvt_pk_bf16_f32 v31, v22, v23
	global_store_dwordx4 v[68:69], v[28:31], off offset:256 nt
	v_lshl_add_u64 v[76:77], s[36:37], 0, v[40:41]
	s_cmp_eq_u32 s2, s88
	s_cbranch_scc1 .Lln2_nx_keep
	s_mov_b32 s88, s2
	s_lshl_b32 s86, s97, 13
	v_mbcnt_lo_u32_b32 v173, -1, 0
	v_mbcnt_hi_u32_b32 v173, -1, v173
	v_lshl_add_u32 v173, v173, 4, s86
	v_add_u32_e32 v191, 16, v40
	v_add_u32_e32 v224, 0x200, v40
	v_add_u32_e32 v225, 0x210, v40
	s_mov_b32 m0, s86
	s_nop 0
	global_load_lds_dwordx4 v191, s[2:3]
	s_add_i32 s87, s86, 0x400
	s_mov_b32 m0, s87
	s_nop 0
	global_load_lds_dwordx4 v40, s[2:3]
	s_add_i32 s87, s86, 0x800
	s_mov_b32 m0, s87
	s_nop 0
	global_load_lds_dwordx4 v191, s[36:37]
	s_add_i32 s87, s86, 0xc00
	s_mov_b32 m0, s87
	s_nop 0
	global_load_lds_dwordx4 v40, s[36:37]
	s_add_i32 s87, s86, 0x1000
	s_mov_b32 m0, s87
	s_nop 0
	global_load_lds_dwordx4 v225, s[2:3]
	s_add_i32 s87, s86, 0x1400
	s_mov_b32 m0, s87
	s_nop 0
	global_load_lds_dwordx4 v224, s[2:3]
	s_add_i32 s87, s86, 0x1800
	s_mov_b32 m0, s87
	s_nop 0
	global_load_lds_dwordx4 v225, s[36:37]
	s_add_i32 s87, s86, 0x1c00
	s_mov_b32 m0, s87
	s_nop 0
	global_load_lds_dwordx4 v224, s[36:37]
	s_waitcnt vmcnt(0)
.Lln2_nx_keep:
	ds_read_b128 v[68:71], v173
	ds_read_b128 v[28:31], v173 offset:1024
	ds_read_b128 v[72:75], v173 offset:2048
	s_nop 0
	ds_read_b128 v[76:79], v173 offset:3072
	s_waitcnt vmcnt(0) lgkmcnt(0)
	v_pk_add_f32 v[76:77], v[76:77], 1.0 op_sel_hi:[1,0]
	s_nop 0
	v_pk_fma_f32 v[28:29], v[16:17], v[76:77], v[28:29]
	v_pk_add_f32 v[76:77], v[78:79], 1.0 op_sel_hi:[1,0]
	v_cvt_pk_bf16_f32 v28, v28, v29
	v_pk_fma_f32 v[30:31], v[18:19], v[76:77], v[30:31]
	s_nop 0
	v_cvt_pk_bf16_f32 v29, v30, v31
	v_pk_add_f32 v[30:31], v[72:73], 1.0 op_sel_hi:[1,0]
	s_nop 0
	v_pk_fma_f32 v[30:31], v[12:13], v[30:31], v[68:69]
	v_pk_add_f32 v[68:69], v[74:75], 1.0 op_sel_hi:[1,0]
	v_cvt_pk_bf16_f32 v30, v30, v31
	v_pk_fma_f32 v[68:69], v[14:15], v[68:69], v[70:71]
	s_nop 0
	v_cvt_pk_bf16_f32 v31, v68, v69
	ds_read_b128 v[68:71], v173 offset:4096
	ds_read_b128 v[72:75], v173 offset:5120
	v_lshl_add_u64 v[80:81], v[38:39], 2, s[36:37]
	ds_read_b128 v[76:79], v173 offset:6144
	s_nop 0
	ds_read_b128 v[80:83], v173 offset:7168
	s_mov_b64 s[36:37], 0
	s_waitcnt vmcnt(0) lgkmcnt(0)
	v_pk_add_f32 v[80:81], v[80:81], 1.0 op_sel_hi:[1,0]
	s_nop 0
	v_pk_fma_f32 v[72:73], v[24:25], v[80:81], v[72:73]
	v_pk_add_f32 v[80:81], v[82:83], 1.0 op_sel_hi:[1,0]
	v_cvt_pk_bf16_f32 v72, v72, v73
	v_pk_fma_f32 v[74:75], v[26:27], v[80:81], v[74:75]
	s_nop 0
	v_cvt_pk_bf16_f32 v73, v74, v75
	v_pk_add_f32 v[74:75], v[76:77], 1.0 op_sel_hi:[1,0]
	s_nop 0
	v_pk_fma_f32 v[68:69], v[20:21], v[74:75], v[68:69]
	s_nop 0
	v_cvt_pk_bf16_f32 v74, v68, v69
	v_pk_add_f32 v[68:69], v[78:79], 1.0 op_sel_hi:[1,0]
	s_nop 0
	v_pk_fma_f32 v[68:69], v[22:23], v[68:69], v[70:71]
	s_nop 0
	v_cvt_pk_bf16_f32 v75, v68, v69
	v_add_co_u32_e32 v68, vcc, 0x11b00000, v84
	s_nop 1
	v_addc_co_u32_e32 v69, vcc, 0, v85, vcc
	global_store_dwordx4 v[68:69], v[28:31], off
	global_store_dwordx4 v[68:69], v[72:75], off offset:256
